# prep_tok rdsa loads batched; dsaq GEMM moved ahead of the PREP work queues
# baseline (speedup 1.0000x reference)
_Z10fwd_kernel6Params:
	s_mov_b32 s100, 0
	v_writelane_b32 v255, s100, 7
	s_mov_b32 s88, s2
	s_load_dword s2, s[0:1], 0xc0
	v_cmp_gt_u32_e32 vcc, 16, v0
	s_waitcnt lgkmcnt(0)
	v_writelane_b32 v252, s2, 0
	s_add_u32 s2, s0, 0xc0
	s_addc_u32 s3, s1, 0
	v_writelane_b32 v252, s2, 1
	s_nop 1
	v_writelane_b32 v252, s3, 2
	s_and_saveexec_b64 s[2:3], vcc
	v_lshl_add_u32 v1, v0, 2, 0
	v_add_u32_e32 v1, 0x21000, v1
	v_mov_b32_e32 v2, 0
	ds_write_b32 v1, v2
	s_or_b64 exec, exec, s[2:3]
	s_load_dwordx4 s[84:87], s[0:1], 0xa8
	v_cmp_gt_u32_e32 vcc, 21, v0
	s_and_saveexec_b64 s[2:3], vcc
	s_cbranch_execz .LBB0_4
	v_lshlrev_b32_e32 v1, 3, v0
	global_load_dwordx2 v[2:3], v1, s[0:1]
	v_add_u32_e32 v1, 0, v1
	v_add_u32_e32 v1, 0x21040, v1
	s_waitcnt vmcnt(0)
	ds_write_b64 v1, v[2:3]

.Lprep_after_cfox:
	s_mov_b32 s100, 1
	v_writelane_b32 v255, s100, 7
	s_branch .LBB0_404

.LBB0_390:
	v_add_u32_e32 v1, s12, v13
	v_ashrrev_i32_e32 v2, 6, v1
	v_add_u32_e32 v22, s9, v2
	v_add_lshl_u32 v26, v2, s8, 6
	v_mad_i64_i32 v[8:9], s[14:15], v22, s24, v[14:15]
	v_ashrrev_i32_e32 v27, 31, v26
	global_load_dwordx4 v[4:7], v[8:9], off
	s_nop 0
	global_load_dwordx4 v[8:11], v[8:9], off offset:128
	v_lshlrev_b64 v[34:35], 2, v[26:27]
	v_lshl_add_u64 v[30:31], v[16:17], 0, v[34:35]
	v_lshl_add_u64 v[38:39], v[18:19], 0, v[34:35]
	global_load_dwordx4 v[26:29], v[30:31], off
	s_nop 0
	global_load_dwordx4 v[30:33], v[30:31], off offset:16
	s_nop 0
	global_load_dwordx4 v[34:37], v[38:39], off
	s_nop 0
	global_load_dwordx4 v[38:41], v[38:39], off offset:16
	v_ashrrev_i32_e32 v23, 31, v22
	v_lshlrev_b64 v[22:23], 10, v[22:23]
	v_add_u32_e32 v1, 0x200, v1
	v_lshl_add_u64 v[22:23], v[20:21], 0, v[22:23]
	v_ashrrev_i32_e32 v1, 6, v1
	s_addk_i32 s12, 0x400
	s_cmpk_eq_i32 s12, 0x1000
	s_waitcnt vmcnt(0) lgkmcnt(0)
	v_lshlrev_b32_e32 v42, 16, v4
	v_and_b32_e32 v43, 0xffff0000, v4
	v_lshlrev_b32_e32 v44, 16, v8
	v_and_b32_e32 v45, 0xffff0000, v8
	v_pk_mul_f32 v[46:47], v[34:35], v[44:45]
	v_pk_mul_f32 v[34:35], v[34:35], v[42:43]
	v_pk_fma_f32 v[46:47], v[26:27], v[42:43], v[46:47] neg_lo:[0,0,1] neg_hi:[0,0,1]
	v_pk_fma_f32 v[26:27], v[26:27], v[44:45], v[34:35]
	v_lshlrev_b32_e32 v34, 16, v9
	v_and_b32_e32 v35, 0xffff0000, v9
	v_cvt_pk_bf16_f32 v8, v26, v27
	v_lshlrev_b32_e32 v26, 16, v5
	v_and_b32_e32 v27, 0xffff0000, v5
	v_pk_mul_f32 v[42:43], v[36:37], v[34:35]
	v_cvt_pk_bf16_f32 v4, v46, v47
	v_pk_fma_f32 v[42:43], v[28:29], v[26:27], v[42:43] neg_lo:[0,0,1] neg_hi:[0,0,1]
	v_pk_mul_f32 v[26:27], v[36:37], v[26:27]
	v_cvt_pk_bf16_f32 v5, v42, v43
	v_pk_fma_f32 v[26:27], v[28:29], v[34:35], v[26:27]
	v_lshlrev_b32_e32 v28, 16, v10
	v_and_b32_e32 v29, 0xffff0000, v10
	v_cvt_pk_bf16_f32 v9, v26, v27
	v_lshlrev_b32_e32 v26, 16, v6
	v_and_b32_e32 v27, 0xffff0000, v6
	v_pk_mul_f32 v[34:35], v[38:39], v[28:29]
	s_nop 0
	v_pk_fma_f32 v[34:35], v[30:31], v[26:27], v[34:35] neg_lo:[0,0,1] neg_hi:[0,0,1]
	v_pk_mul_f32 v[26:27], v[38:39], v[26:27]
	v_cvt_pk_bf16_f32 v6, v34, v35
	v_pk_fma_f32 v[26:27], v[30:31], v[28:29], v[26:27]
	v_lshlrev_b32_e32 v28, 16, v11
	v_and_b32_e32 v29, 0xffff0000, v11
	v_cvt_pk_bf16_f32 v10, v26, v27
	v_lshlrev_b32_e32 v26, 16, v7
	v_and_b32_e32 v27, 0xffff0000, v7
	v_pk_mul_f32 v[30:31], v[40:41], v[28:29]
	s_nop 0
	v_pk_fma_f32 v[30:31], v[32:33], v[26:27], v[30:31] neg_lo:[0,0,1] neg_hi:[0,0,1]
	v_pk_mul_f32 v[26:27], v[40:41], v[26:27]
	v_cvt_pk_bf16_f32 v7, v30, v31
	v_pk_fma_f32 v[26:27], v[32:33], v[28:29], v[26:27]
	s_nop 0
	v_cvt_pk_bf16_f32 v11, v26, v27
	global_store_dwordx4 v[22:23], v[4:7], off
	global_store_dwordx4 v[22:23], v[8:11], off offset:128
	v_add_u32_e32 v22, s9, v1
	v_add_lshl_u32 v26, v1, s8, 6
	v_mad_i64_i32 v[4:5], s[14:15], v22, s24, v[14:15]
	v_ashrrev_i32_e32 v27, 31, v26
	global_load_dwordx4 v[8:11], v[4:5], off
	s_nop 0
	global_load_dwordx4 v[4:7], v[4:5], off offset:128
	v_lshlrev_b64 v[34:35], 2, v[26:27]
	v_lshl_add_u64 v[30:31], v[16:17], 0, v[34:35]
	v_lshl_add_u64 v[38:39], v[18:19], 0, v[34:35]
	global_load_dwordx4 v[26:29], v[30:31], off
	s_nop 0
	global_load_dwordx4 v[30:33], v[30:31], off offset:16
	s_nop 0
	global_load_dwordx4 v[34:37], v[38:39], off
	s_nop 0
	global_load_dwordx4 v[38:41], v[38:39], off offset:16
	v_ashrrev_i32_e32 v23, 31, v22
	v_lshlrev_b64 v[22:23], 10, v[22:23]
	v_lshl_add_u64 v[22:23], v[20:21], 0, v[22:23]
	s_waitcnt vmcnt(0) lgkmcnt(0)
	v_lshlrev_b32_e32 v42, 16, v8
	v_and_b32_e32 v43, 0xffff0000, v8
	v_lshlrev_b32_e32 v44, 16, v4
	v_and_b32_e32 v45, 0xffff0000, v4
	v_pk_mul_f32 v[46:47], v[34:35], v[44:45]
	v_pk_mul_f32 v[34:35], v[34:35], v[42:43]
	v_pk_fma_f32 v[46:47], v[26:27], v[42:43], v[46:47] neg_lo:[0,0,1] neg_hi:[0,0,1]
	v_pk_fma_f32 v[26:27], v[26:27], v[44:45], v[34:35]
	v_lshlrev_b32_e32 v34, 16, v5
	v_and_b32_e32 v35, 0xffff0000, v5
	v_cvt_pk_bf16_f32 v8, v26, v27
	v_lshlrev_b32_e32 v26, 16, v9
	v_and_b32_e32 v27, 0xffff0000, v9
	v_pk_mul_f32 v[42:43], v[36:37], v[34:35]
	v_cvt_pk_bf16_f32 v4, v46, v47
	v_pk_fma_f32 v[42:43], v[28:29], v[26:27], v[42:43] neg_lo:[0,0,1] neg_hi:[0,0,1]
	v_pk_mul_f32 v[26:27], v[36:37], v[26:27]
	v_cvt_pk_bf16_f32 v5, v42, v43
	v_pk_fma_f32 v[26:27], v[28:29], v[34:35], v[26:27]
	v_lshlrev_b32_e32 v28, 16, v6
	v_and_b32_e32 v29, 0xffff0000, v6
	v_cvt_pk_bf16_f32 v9, v26, v27
	v_lshlrev_b32_e32 v26, 16, v10
	v_and_b32_e32 v27, 0xffff0000, v10
	v_pk_mul_f32 v[34:35], v[38:39], v[28:29]
	s_nop 0
	v_pk_fma_f32 v[34:35], v[30:31], v[26:27], v[34:35] neg_lo:[0,0,1] neg_hi:[0,0,1]
	v_pk_mul_f32 v[26:27], v[38:39], v[26:27]
	v_cvt_pk_bf16_f32 v6, v34, v35
	v_pk_fma_f32 v[26:27], v[30:31], v[28:29], v[26:27]
	v_lshlrev_b32_e32 v28, 16, v7
	v_and_b32_e32 v29, 0xffff0000, v7
	v_cvt_pk_bf16_f32 v10, v26, v27
	v_lshlrev_b32_e32 v26, 16, v11
	v_and_b32_e32 v27, 0xffff0000, v11
	v_pk_mul_f32 v[30:31], v[40:41], v[28:29]
	s_nop 0
	v_pk_fma_f32 v[30:31], v[32:33], v[26:27], v[30:31] neg_lo:[0,0,1] neg_hi:[0,0,1]
	v_pk_mul_f32 v[26:27], v[40:41], v[26:27]
	v_cvt_pk_bf16_f32 v7, v30, v31
	v_pk_fma_f32 v[26:27], v[32:33], v[28:29], v[26:27]
	s_nop 0
	v_cvt_pk_bf16_f32 v11, v26, v27
	global_store_dwordx4 v[22:23], v[4:7], off
	global_store_dwordx4 v[22:23], v[8:11], off offset:128
	s_cbranch_scc0 .LBB0_390
	v_ashrrev_i32_e32 v1, 3, v13
	v_and_b32_e32 v9, 7, v13
	v_add_u32_e32 v8, s9, v1
	v_mov_b64_e32 v[4:5], s[10:11]
	v_mul_u32_u24_e32 v2, 48, v9
	v_mad_i64_i32 v[4:5], s[12:13], v8, s24, v[4:5]
	v_lshlrev_b32_e32 v2, 1, v2
	v_lshl_add_u64 v[6:7], v[4:5], 0, v[2:3]
	s_mov_b64 s[12:13], 0x2c00
	v_lshl_add_u64 v[4:5], v[6:7], 0, s[12:13]
	v_add_co_u32_e32 v6, vcc, 0x2000, v6
	s_nop 1
	v_addc_co_u32_e32 v7, vcc, 0, v7, vcc
	global_load_dwordx4 v[64:67], v[6:7], off offset:3072
	global_load_dwordx4 v[68:71], v[4:5], off offset:16
	global_load_dwordx4 v[72:75], v[4:5], off offset:32
	global_load_dwordx4 v[76:79], v[4:5], off offset:48
	global_load_dwordx4 v[80:83], v[4:5], off offset:64
	global_load_dwordx4 v[84:87], v[4:5], off offset:80
	s_waitcnt vmcnt(0) lgkmcnt(0)
	v_and_b32_e32 v6, 0xffff0000, v64
	v_lshlrev_b32_e32 v2, 16, v64
	v_mul_f32_e32 v6, v6, v6
	v_and_b32_e32 v7, 0xffff0000, v65
	v_fmac_f32_e32 v6, v2, v2
	v_lshlrev_b32_e32 v2, 16, v65
	v_mul_f32_e32 v7, v7, v7
	v_fmac_f32_e32 v7, v2, v2
	v_add_f32_e32 v2, v6, v7
	v_and_b32_e32 v7, 0xffff0000, v66
	v_lshlrev_b32_e32 v6, 16, v66
	v_mul_f32_e32 v7, v7, v7
	v_fmac_f32_e32 v7, v6, v6
	v_add_f32_e32 v2, v7, v2
	v_lshlrev_b32_e32 v6, 16, v67
	v_and_b32_e32 v7, 0xffff0000, v67
	v_mul_f32_e32 v7, v7, v7
	v_fmac_f32_e32 v7, v6, v6
	v_add_f32_e32 v2, v7, v2
	v_and_b32_e32 v7, 0xffff0000, v68
	v_lshlrev_b32_e32 v6, 16, v68
	v_mul_f32_e32 v7, v7, v7
	v_fmac_f32_e32 v7, v6, v6
	v_add_f32_e32 v2, v7, v2
	v_and_b32_e32 v7, 0xffff0000, v69
	v_lshlrev_b32_e32 v6, 16, v69
	v_mul_f32_e32 v7, v7, v7
	v_fmac_f32_e32 v7, v6, v6
	v_add_f32_e32 v2, v7, v2
	v_and_b32_e32 v7, 0xffff0000, v70
	v_lshlrev_b32_e32 v6, 16, v70
	v_mul_f32_e32 v7, v7, v7
	v_fmac_f32_e32 v7, v6, v6
	v_add_f32_e32 v2, v7, v2
	v_lshlrev_b32_e32 v6, 16, v71
	v_and_b32_e32 v7, 0xffff0000, v71
	v_mul_f32_e32 v7, v7, v7
	v_fmac_f32_e32 v7, v6, v6
	v_add_f32_e32 v2, v7, v2
	v_and_b32_e32 v7, 0xffff0000, v72
	v_lshlrev_b32_e32 v6, 16, v72
	v_mul_f32_e32 v7, v7, v7
	v_fmac_f32_e32 v7, v6, v6
	v_add_f32_e32 v2, v7, v2
	v_and_b32_e32 v7, 0xffff0000, v73
	v_lshlrev_b32_e32 v6, 16, v73
	v_mul_f32_e32 v7, v7, v7
	v_fmac_f32_e32 v7, v6, v6
	v_add_f32_e32 v2, v7, v2
	v_and_b32_e32 v7, 0xffff0000, v74
	v_lshlrev_b32_e32 v6, 16, v74
	v_mul_f32_e32 v7, v7, v7
	v_fmac_f32_e32 v7, v6, v6
	v_add_f32_e32 v2, v7, v2
	v_lshlrev_b32_e32 v6, 16, v75
	v_and_b32_e32 v7, 0xffff0000, v75
	v_mul_f32_e32 v7, v7, v7
	v_fmac_f32_e32 v7, v6, v6
	v_add_f32_e32 v2, v7, v2
	v_and_b32_e32 v7, 0xffff0000, v76
	v_lshlrev_b32_e32 v6, 16, v76
	v_mul_f32_e32 v7, v7, v7
	v_fmac_f32_e32 v7, v6, v6
	v_add_f32_e32 v2, v7, v2
	v_and_b32_e32 v7, 0xffff0000, v77
	v_lshlrev_b32_e32 v6, 16, v77
	v_mul_f32_e32 v7, v7, v7
	v_fmac_f32_e32 v7, v6, v6
	v_add_f32_e32 v2, v7, v2
	v_and_b32_e32 v7, 0xffff0000, v78
	v_lshlrev_b32_e32 v6, 16, v78
	v_mul_f32_e32 v7, v7, v7
	v_fmac_f32_e32 v7, v6, v6
	v_add_f32_e32 v2, v7, v2
	v_lshlrev_b32_e32 v6, 16, v79
	v_and_b32_e32 v7, 0xffff0000, v79
	v_mul_f32_e32 v7, v7, v7
	v_fmac_f32_e32 v7, v6, v6
	v_add_f32_e32 v2, v7, v2
	v_and_b32_e32 v7, 0xffff0000, v80
	v_lshlrev_b32_e32 v6, 16, v80
	v_mul_f32_e32 v7, v7, v7
	v_fmac_f32_e32 v7, v6, v6
	v_add_f32_e32 v2, v7, v2
	v_and_b32_e32 v7, 0xffff0000, v81
	v_lshlrev_b32_e32 v6, 16, v81
	v_mul_f32_e32 v7, v7, v7
	v_fmac_f32_e32 v7, v6, v6
	v_add_f32_e32 v2, v7, v2
	v_and_b32_e32 v7, 0xffff0000, v82
	v_lshlrev_b32_e32 v6, 16, v82
	v_mul_f32_e32 v7, v7, v7
	v_fmac_f32_e32 v7, v6, v6
	v_add_f32_e32 v2, v7, v2
	v_and_b32_e32 v7, 0xffff0000, v83
	v_lshlrev_b32_e32 v6, 16, v83
	v_mul_f32_e32 v7, v7, v7
	v_fmac_f32_e32 v7, v6, v6
	v_add_f32_e32 v2, v7, v2
	v_lshlrev_b32_e32 v10, 16, v84
	v_and_b32_e32 v84, 0xffff0000, v84
	v_mul_f32_e32 v84, v84, v84
	v_fmac_f32_e32 v84, v10, v10
	v_add_f32_e32 v2, v84, v2
	v_lshlrev_b32_e32 v84, 16, v85
	v_and_b32_e32 v85, 0xffff0000, v85
	v_mul_f32_e32 v85, v85, v85
	v_fmac_f32_e32 v85, v84, v84
	v_add_f32_e32 v2, v85, v2
	v_and_b32_e32 v85, 0xffff0000, v86
	v_lshlrev_b32_e32 v84, 16, v86
	v_mul_f32_e32 v85, v85, v85
	v_fmac_f32_e32 v85, v84, v84
	v_add_f32_e32 v2, v85, v2
	v_and_b32_e32 v85, 0xffff0000, v87
	v_lshlrev_b32_e32 v84, 16, v87
	v_mul_f32_e32 v85, v85, v85
	v_fmac_f32_e32 v85, v84, v84
	v_mbcnt_hi_u32_b32 v4, -1, v251
	v_and_b32_e32 v6, 64, v4
	v_add_f32_e32 v2, v85, v2
	v_xor_b32_e32 v5, 1, v4
	v_add_u32_e32 v6, 64, v6
	v_cmp_lt_i32_e32 vcc, v5, v6
	s_nop 1
	v_cndmask_b32_e32 v5, v4, v5, vcc
	v_lshlrev_b32_e32 v5, 2, v5
	ds_bpermute_b32 v5, v5, v2
	s_waitcnt lgkmcnt(0)
	v_add_f32_e32 v2, v2, v5
	v_xor_b32_e32 v5, 2, v4
	v_cmp_lt_i32_e32 vcc, v5, v6
	s_nop 1
	v_cndmask_b32_e32 v5, v4, v5, vcc
	v_lshlrev_b32_e32 v5, 2, v5
	ds_bpermute_b32 v5, v5, v2
	s_waitcnt lgkmcnt(0)
	v_add_f32_e32 v2, v2, v5
	v_xor_b32_e32 v5, 4, v4
	v_cmp_lt_i32_e32 vcc, v5, v6
	s_nop 1
	v_cndmask_b32_e32 v4, v4, v5, vcc
	v_lshlrev_b32_e32 v4, 2, v4
	ds_bpermute_b32 v4, v4, v2
	v_cmp_eq_u32_e32 vcc, 0, v9
	s_and_saveexec_b64 s[12:13], vcc
	s_cbranch_execz .LBB0_384
	s_waitcnt lgkmcnt(0)
	v_add_f32_e32 v2, v2, v4
	v_fmamk_f32 v2, v2, 0x3b2aaaab, v241
	v_mul_f32_e32 v4, 0x4b800000, v2
	v_cmp_gt_f32_e32 vcc, s25, v2
	v_ashrrev_i32_e32 v9, 31, v8
	s_nop 0
	v_cndmask_b32_e32 v2, v2, v4, vcc
	v_rsq_f32_e32 v2, v2
	v_lshl_add_u64 v[4:5], v[8:9], 2, s[4:5]
	v_mul_f32_e32 v6, 0x45800000, v2
	v_cndmask_b32_e32 v2, v2, v6, vcc
	v_add_co_u32_e32 v4, vcc, 0x49240000, v4
	s_nop 1
	v_addc_co_u32_e32 v5, vcc, 0, v5, vcc
	global_store_dword v[4:5], v2, off
	s_branch .LBB0_384

.LBB0_424:
	v_readlane_b32 s100, v255, 7
	s_nop 3
	s_cmp_eq_u32 s100, 1
	s_cbranch_scc0 .Lprep_dsaq_done
	s_mov_b32 s100, 0
	v_writelane_b32 v255, s100, 7
	s_branch .Lprep_main
